# v-epoch loop rewritten on the matrix cores: rows staged in LDS, ds_read_b64_tr_b4 transposed reads, f8f6f4 MFMA with 3-term fp8 weights, f32 accumulation
# speedup vs baseline: 1.0421x; 1.0421x over previous
; #define LAS __attribute__((address_space(3)))
; __device__ __forceinline__ void expert_phase(const Frame& F, int l, int xcc, LAS unsigned char* wl, const LAS unsigned char* zb) {
;     ...
;             auto v_rows = [&](int i, URows& R) {
;                 const unsigned char* Vsl = VBl + (size_t)slice_of(i) * XSL_BYTES;
;                 const u32x4 ia = *(const LAS u32x4*)(IDL + (i & 7) * 256 + rr * 32), ib = *(const LAS u32x4*)(IDL + (i & 7) * 256 + rr * 32 + 16);
; #pragma unroll
;                 for (int j = 0; j < 16; ++j) { const unsigned w = j < 8 ? ia[(j >> 1) & 3] : ib[(j >> 1) & 3]; const unsigned e = (j & 1) ? (w >> 16) : (w & 0xffffu);
;                     R.r[j] = ldo_u4(Vsl, e * 128u + 16u * pc); }
;             };
;             auto v_comp = [&](int i, const URows& R) {
;                 const int k = i & 7, t = tok(k), sl = slice_of(i);
;                 const unsigned col = 32u * pc + 4u * rr;
;                 u32x2 xw;
;                 typedef _Float16 hf2 __attribute__((ext_vector_type(2)));
;                 const LAS u32x4* wp = (const LAS u32x4*)(SA + k * 256 + 16 * rr);
;                 const u32x4 wall[4] = {wp[0], wp[1], wp[2], wp[3]};
;                 unsigned out[16];
; #pragma unroll
;                 for (int j = 0; j < 16; ++j) out[j] = 0u;
; #pragma unroll
;                 for (int j = 0; j < 16; ++j) {
;                     if (j == 8) xw = ldo_u2(X1 + (size_t)t * D + sl * 256, 2u * col);
;                     u32x4 rj = R.r[j];
;                     asm volatile("" : "+v"(rj.x), "+v"(rj.y), "+v"(rj.z), "+v"(rj.w) :: "memory");
;                     const unsigned wj = wall[j >> 2][j & 3]; const hf2 w2 = __builtin_bit_cast(hf2, wj);
; #pragma unroll
;                     for (int d = 0; d < 4; ++d) {
;                         const hf2 a = __builtin_amdgcn_cvt_scalef32_pk_f16_fp4(rj[d], 1.0f, 0), b = __builtin_amdgcn_cvt_scalef32_pk_f16_fp4(rj[d], 1.0f, 1),
;                                   cc = __builtin_amdgcn_cvt_scalef32_pk_f16_fp4(rj[d], 1.0f, 2), dd = __builtin_amdgcn_cvt_scalef32_pk_f16_fp4(rj[d], 1.0f, 3);
;                         out[4 * d] = __builtin_bit_cast(unsigned, __builtin_elementwise_fma(a, w2, __builtin_bit_cast(hf2, out[4 * d])));
;                         out[4 * d + 1] = __builtin_bit_cast(unsigned, __builtin_elementwise_fma(b, w2, __builtin_bit_cast(hf2, out[4 * d + 1])));
.LBB0_1239:
	s_or_b64 exec, exec, s[2:3]
	s_waitcnt vmcnt(0) lgkmcnt(0)
	v_and_b32_e32 v120, 7, v211
	v_lshrrev_b32_e32 v121, 3, v211
	v_and_b32_e32 v122, 15, v211
	v_lshrrev_b32_e32 v123, 4, v211
	s_lshr_b32 s2, s83, 10
	s_mul_i32 s2, s2, 79
	s_lshr_b32 s2, s2, 10
	s_mul_i32 s3, s2, 0x1200
	s_mov_b32 s8, 0x1c200
	s_mov_b32 s9, 0x1cc00
	s_cmp_lt_u32 s2, 3
	s_cselect_b32 s8, s8, s9
	s_mov_b32 s9, 0x1d400
	s_cmp_lt_u32 s2, 6
	s_cselect_b32 s8, s8, s9
	s_add_i32 s3, s3, s8
	v_lshlrev_b32_e32 v113, 4, v120
	v_mul_u32_u24_e32 v110, 0x240, v121
	v_add3_u32 v110, v110, v113, s3
	v_mul_u32_u24_e32 v111, 0x90, v122
	v_lshl_add_u32 v111, v123, 3, v111
	v_add_u32_e32 v111, s3, v111
	v_lshlrev_b32_e32 v112, 3, v121
	v_add_u32_e32 v112, s83, v112
	v_add_u32_e32 v112, 0x2a40, v112
	v_lshrrev_b32_e32 v124, 2, v122
	v_and_b32_e32 v125, 1, v123
	v_lshlrev_b32_e32 v114, 7, v124
	v_lshl_add_u32 v114, v125, 4, v114
	v_add_u32_e32 v114, s83, v114
	v_add_u32_e32 v114, 0x200, v114
	v_and_b32_e32 v126, 3, v211
	v_lshlrev_b32_e32 v115, 6, v126
	v_lshl_add_u32 v115, v123, 4, v115
	v_add_u32_e32 v115, s3, v115
	v_lshl_add_u32 v116, v211, 4, s3
	v_lshl_add_u32 v117, v211, 2, s83
	v_add_u32_e32 v117, 0x2000, v117
	v_lshl_add_u32 v118, v211, 2, s83
	v_add_u32_e32 v119, s83, v211
	v_add_u32_e32 v119, 0x200, v119
	s_mov_b32 s30, 0x1110111
	s_mov_b32 s31, 0x2220222
	s_mov_b32 s44, 0x4440444
	s_mov_b32 s45, 0x8880888
	s_mov_b32 s100, 0xf000f
	s_mov_b32 s101, 0xf000f
	s_mov_b32 s77, 0x7fff80
	s_mov_b32 s66, 0x07060302
	s_mov_b32 s68, 0x7fff
	ds_read2st64_b32 v[120:121], v118 offset0:0 offset1:1
	s_waitcnt lgkmcnt(0)
	v_cvt_f32_f16_e32 v122, v120
	v_cvt_f32_f16_e32 v123, v121
	v_cvt_pk_fp8_f32 v124, v122, v122
	v_cvt_pk_fp8_f32 v125, v123, v123
	s_nop 0
	ds_write_b8 v119, v124 offset:0
	ds_write_b8 v119, v125 offset:64
	v_cvt_f32_fp8_e32 v126, v124
	v_cvt_f32_fp8_e32 v127, v125
	s_nop 0
	v_sub_f32_e32 v128, v122, v126
	v_sub_f32_e32 v129, v123, v127
	v_cvt_pk_fp8_f32 v124, v128, v128
	v_cvt_pk_fp8_f32 v125, v129, v129
	s_nop 0
	ds_write_b8 v119, v124 offset:128
	ds_write_b8 v119, v125 offset:192
	v_cvt_f32_fp8_e32 v126, v124
	v_cvt_f32_fp8_e32 v127, v125
	s_nop 0
	v_sub_f32_e32 v128, v128, v126
	v_sub_f32_e32 v129, v129, v127
	v_cvt_pk_fp8_f32 v124, v128, v128
	v_cvt_pk_fp8_f32 v125, v129, v129
	s_nop 0
	ds_write_b8 v119, v124 offset:256
	ds_write_b8 v119, v125 offset:320
	ds_read2st64_b32 v[120:121], v118 offset0:4 offset1:5
	s_waitcnt lgkmcnt(0)
	v_cvt_f32_f16_e32 v122, v120
	v_cvt_f32_f16_e32 v123, v121
	v_cvt_pk_fp8_f32 v124, v122, v122
	v_cvt_pk_fp8_f32 v125, v123, v123
	s_nop 0
	ds_write_b8 v119, v124 offset:1024
	ds_write_b8 v119, v125 offset:1088
	v_cvt_f32_fp8_e32 v126, v124
	v_cvt_f32_fp8_e32 v127, v125
	s_nop 0
	v_sub_f32_e32 v128, v122, v126
	v_sub_f32_e32 v129, v123, v127
	v_cvt_pk_fp8_f32 v124, v128, v128
	v_cvt_pk_fp8_f32 v125, v129, v129
	s_nop 0
	ds_write_b8 v119, v124 offset:1152
	ds_write_b8 v119, v125 offset:1216
	v_cvt_f32_fp8_e32 v126, v124
	v_cvt_f32_fp8_e32 v127, v125
	s_nop 0
	v_sub_f32_e32 v128, v128, v126
	v_sub_f32_e32 v129, v129, v127
	v_cvt_pk_fp8_f32 v124, v128, v128
	v_cvt_pk_fp8_f32 v125, v129, v129
	s_nop 0
	ds_write_b8 v119, v124 offset:1280
	ds_write_b8 v119, v125 offset:1344
	ds_read2st64_b32 v[120:121], v118 offset0:8 offset1:9
	s_waitcnt lgkmcnt(0)
	v_cvt_f32_f16_e32 v122, v120
	v_cvt_f32_f16_e32 v123, v121
	v_cvt_pk_fp8_f32 v124, v122, v122
	v_cvt_pk_fp8_f32 v125, v123, v123
	s_nop 0
	ds_write_b8 v119, v124 offset:2048
	ds_write_b8 v119, v125 offset:2112
	v_cvt_f32_fp8_e32 v126, v124
	v_cvt_f32_fp8_e32 v127, v125
	s_nop 0
	v_sub_f32_e32 v128, v122, v126
	v_sub_f32_e32 v129, v123, v127
	v_cvt_pk_fp8_f32 v124, v128, v128
	v_cvt_pk_fp8_f32 v125, v129, v129
	s_nop 0
	ds_write_b8 v119, v124 offset:2176
	ds_write_b8 v119, v125 offset:2240
	v_cvt_f32_fp8_e32 v126, v124
	v_cvt_f32_fp8_e32 v127, v125
	s_nop 0
	v_sub_f32_e32 v128, v128, v126
	v_sub_f32_e32 v129, v129, v127
	v_cvt_pk_fp8_f32 v124, v128, v128
	v_cvt_pk_fp8_f32 v125, v129, v129
	s_nop 0
	ds_write_b8 v119, v124 offset:2304
	ds_write_b8 v119, v125 offset:2368
	ds_read2st64_b32 v[120:121], v118 offset0:12 offset1:13
	s_waitcnt lgkmcnt(0)
	v_cvt_f32_f16_e32 v122, v120
	v_cvt_f32_f16_e32 v123, v121
	v_cvt_pk_fp8_f32 v124, v122, v122
	v_cvt_pk_fp8_f32 v125, v123, v123
	s_nop 0
	ds_write_b8 v119, v124 offset:3072
	ds_write_b8 v119, v125 offset:3136
	v_cvt_f32_fp8_e32 v126, v124
	v_cvt_f32_fp8_e32 v127, v125
	s_nop 0
	v_sub_f32_e32 v128, v122, v126
	v_sub_f32_e32 v129, v123, v127
	v_cvt_pk_fp8_f32 v124, v128, v128
	v_cvt_pk_fp8_f32 v125, v129, v129
	s_nop 0
	ds_write_b8 v119, v124 offset:3200
	ds_write_b8 v119, v125 offset:3264
	v_cvt_f32_fp8_e32 v126, v124
	v_cvt_f32_fp8_e32 v127, v125
	s_nop 0
	v_sub_f32_e32 v128, v128, v126
	v_sub_f32_e32 v129, v129, v127
	v_cvt_pk_fp8_f32 v124, v128, v128
	v_cvt_pk_fp8_f32 v125, v129, v129
	s_nop 0
	ds_write_b8 v119, v124 offset:3328
	ds_write_b8 v119, v125 offset:3392
	ds_read2st64_b32 v[120:121], v118 offset0:16 offset1:17
	s_waitcnt lgkmcnt(0)
	v_cvt_f32_f16_e32 v122, v120
	v_cvt_f32_f16_e32 v123, v121
	v_cvt_pk_fp8_f32 v124, v122, v122
	v_cvt_pk_fp8_f32 v125, v123, v123
	s_nop 0
	ds_write_b8 v119, v124 offset:4096
	ds_write_b8 v119, v125 offset:4160
	v_cvt_f32_fp8_e32 v126, v124
	v_cvt_f32_fp8_e32 v127, v125
	s_nop 0
	v_sub_f32_e32 v128, v122, v126
	v_sub_f32_e32 v129, v123, v127
	v_cvt_pk_fp8_f32 v124, v128, v128
	v_cvt_pk_fp8_f32 v125, v129, v129
	s_nop 0
	ds_write_b8 v119, v124 offset:4224
	ds_write_b8 v119, v125 offset:4288
	v_cvt_f32_fp8_e32 v126, v124
	v_cvt_f32_fp8_e32 v127, v125
	s_nop 0
	v_sub_f32_e32 v128, v128, v126
	v_sub_f32_e32 v129, v129, v127
	v_cvt_pk_fp8_f32 v124, v128, v128
	v_cvt_pk_fp8_f32 v125, v129, v129
	s_nop 0
	ds_write_b8 v119, v124 offset:4352
	ds_write_b8 v119, v125 offset:4416
	ds_read2st64_b32 v[120:121], v118 offset0:20 offset1:21
	s_waitcnt lgkmcnt(0)
; #define LAS __attribute__((address_space(3)))
; #define XFENCE() asm volatile("" ::: "memory")
; __device__ __forceinline__ void expert_phase(const Frame& F, int l, int xcc, LAS unsigned char* wl, const LAS unsigned char* zb) {
;     ...
;             auto v_rows = [&](int i, URows& R) {
;                 const unsigned char* Vsl = VBl + (size_t)slice_of(i) * XSL_BYTES;
;                 const u32x4 ia = *(const LAS u32x4*)(IDL + (i & 7) * 256 + rr * 32), ib = *(const LAS u32x4*)(IDL + (i & 7) * 256 + rr * 32 + 16);
; #pragma unroll
;                 for (int j = 0; j < 16; ++j) { const unsigned w = j < 8 ? ia[(j >> 1) & 3] : ib[(j >> 1) & 3]; const unsigned e = (j & 1) ? (w >> 16) : (w & 0xffffu);
;                     R.r[j] = ldo_u4(Vsl, e * 128u + 16u * pc); }
;             };
;     ...
;             URows RA, RB;
;             v_rows(0, RA);
;             XFENCE();
; #pragma unroll 1
;             for (int i = 0; i < 64; i += 2) {
;                 const int i2 = i + 2 < 64 ? i + 2 : 63;
;                 v_rows(i + 1, RB);
	v_cvt_f32_f16_e32 v122, v120
	v_cvt_f32_f16_e32 v123, v121
	v_cvt_pk_fp8_f32 v124, v122, v122
	v_cvt_pk_fp8_f32 v125, v123, v123
	s_nop 0
	ds_write_b8 v119, v124 offset:5120
	ds_write_b8 v119, v125 offset:5184
	v_cvt_f32_fp8_e32 v126, v124
	v_cvt_f32_fp8_e32 v127, v125
	s_nop 0
	v_sub_f32_e32 v128, v122, v126
	v_sub_f32_e32 v129, v123, v127
	v_cvt_pk_fp8_f32 v124, v128, v128
	v_cvt_pk_fp8_f32 v125, v129, v129
	s_nop 0
	ds_write_b8 v119, v124 offset:5248
	ds_write_b8 v119, v125 offset:5312
	v_cvt_f32_fp8_e32 v126, v124
	v_cvt_f32_fp8_e32 v127, v125
	s_nop 0
	v_sub_f32_e32 v128, v128, v126
	v_sub_f32_e32 v129, v129, v127
	v_cvt_pk_fp8_f32 v124, v128, v128
	v_cvt_pk_fp8_f32 v125, v129, v129
	s_nop 0
	ds_write_b8 v119, v124 offset:5376
	ds_write_b8 v119, v125 offset:5440
	ds_read2st64_b32 v[120:121], v118 offset0:24 offset1:25
	s_waitcnt lgkmcnt(0)
	v_cvt_f32_f16_e32 v122, v120
	v_cvt_f32_f16_e32 v123, v121
	v_cvt_pk_fp8_f32 v124, v122, v122
	v_cvt_pk_fp8_f32 v125, v123, v123
	s_nop 0
	ds_write_b8 v119, v124 offset:6144
	ds_write_b8 v119, v125 offset:6208
	v_cvt_f32_fp8_e32 v126, v124
	v_cvt_f32_fp8_e32 v127, v125
	s_nop 0
	v_sub_f32_e32 v128, v122, v126
	v_sub_f32_e32 v129, v123, v127
	v_cvt_pk_fp8_f32 v124, v128, v128
	v_cvt_pk_fp8_f32 v125, v129, v129
	s_nop 0
	ds_write_b8 v119, v124 offset:6272
	ds_write_b8 v119, v125 offset:6336
	v_cvt_f32_fp8_e32 v126, v124
	v_cvt_f32_fp8_e32 v127, v125
	s_nop 0
	v_sub_f32_e32 v128, v128, v126
	v_sub_f32_e32 v129, v129, v127
	v_cvt_pk_fp8_f32 v124, v128, v128
	v_cvt_pk_fp8_f32 v125, v129, v129
	s_nop 0
	ds_write_b8 v119, v124 offset:6400
	ds_write_b8 v119, v125 offset:6464
	ds_read2st64_b32 v[120:121], v118 offset0:28 offset1:29
	s_waitcnt lgkmcnt(0)
	v_cvt_f32_f16_e32 v122, v120
	v_cvt_f32_f16_e32 v123, v121
	v_cvt_pk_fp8_f32 v124, v122, v122
	v_cvt_pk_fp8_f32 v125, v123, v123
	s_nop 0
	ds_write_b8 v119, v124 offset:7168
	ds_write_b8 v119, v125 offset:7232
	v_cvt_f32_fp8_e32 v126, v124
	v_cvt_f32_fp8_e32 v127, v125
	s_nop 0
	v_sub_f32_e32 v128, v122, v126
	v_sub_f32_e32 v129, v123, v127
	v_cvt_pk_fp8_f32 v124, v128, v128
	v_cvt_pk_fp8_f32 v125, v129, v129
	s_nop 0
	ds_write_b8 v119, v124 offset:7296
	ds_write_b8 v119, v125 offset:7360
	v_cvt_f32_fp8_e32 v126, v124
	v_cvt_f32_fp8_e32 v127, v125
	s_nop 0
	v_sub_f32_e32 v128, v128, v126
	v_sub_f32_e32 v129, v129, v127
	v_cvt_pk_fp8_f32 v124, v128, v128
	v_cvt_pk_fp8_f32 v125, v129, v129
	s_nop 0
	ds_write_b8 v119, v124 offset:7424
	ds_write_b8 v119, v125 offset:7488
	s_mov_b32 s67, 0
	s_and_b32 s33, s67, 7
	s_lshr_b32 s58, s67, 3
	s_add_i32 s58, s58, s96
	s_and_b32 s58, s58, 7
	s_mul_i32 s8, s33, s82
	s_add_i32 s8, s8, s26
	s_cmpk_lt_i32 s8, 0x4000
	s_cselect_b32 s8, s8, s26
	s_lshl_b32 s78, s58, 21
	s_add_u32 s64, s57, s78
	s_addc_u32 s65, s70, 0
	s_lshl_b32 s78, s33, 8
	v_add_u32_e32 v123, s78, v112
	ds_read_b64 v[108:109], v123 offset:0
	s_waitcnt lgkmcnt(0)
	v_lshlrev_b32_e32 v208, 7, v108
	v_and_or_b32 v208, v208, s77, v113
	global_load_dwordx4 v[0:3], v208, s[64:65]
	v_bfe_u32 v209, v108, 16, 16
	v_lshl_or_b32 v209, v209, 7, v113
	global_load_dwordx4 v[4:7], v209, s[64:65]
	v_lshlrev_b32_e32 v208, 7, v109
	v_and_or_b32 v208, v208, s77, v113
	global_load_dwordx4 v[8:11], v208, s[64:65]
	v_bfe_u32 v209, v109, 16, 16
	v_lshl_or_b32 v209, v209, 7, v113
	global_load_dwordx4 v[12:15], v209, s[64:65]
	s_lshl_b32 s78, s33, 8
	v_add_u32_e32 v123, s78, v112
	ds_read_b64 v[108:109], v123 offset:64
	s_waitcnt lgkmcnt(0)
	v_lshlrev_b32_e32 v208, 7, v108
	v_and_or_b32 v208, v208, s77, v113
	global_load_dwordx4 v[16:19], v208, s[64:65]
	v_bfe_u32 v209, v108, 16, 16
	v_lshl_or_b32 v209, v209, 7, v113
	global_load_dwordx4 v[20:23], v209, s[64:65]
	v_lshlrev_b32_e32 v208, 7, v109
	v_and_or_b32 v208, v208, s77, v113
	global_load_dwordx4 v[24:27], v208, s[64:65]
	v_bfe_u32 v209, v109, 16, 16
	v_lshl_or_b32 v209, v209, 7, v113
	global_load_dwordx4 v[28:31], v209, s[64:65]
	s_lshl_b32 s78, s33, 8
	v_add_u32_e32 v123, s78, v112
	ds_read_b64 v[108:109], v123 offset:128
	s_waitcnt lgkmcnt(0)
	v_lshlrev_b32_e32 v208, 7, v108
	v_and_or_b32 v208, v208, s77, v113
	global_load_dwordx4 v[32:35], v208, s[64:65]
	v_bfe_u32 v209, v108, 16, 16
	v_lshl_or_b32 v209, v209, 7, v113
	global_load_dwordx4 v[36:39], v209, s[64:65]
	v_lshlrev_b32_e32 v208, 7, v109
	v_and_or_b32 v208, v208, s77, v113
	global_load_dwordx4 v[40:43], v208, s[64:65]
	v_bfe_u32 v209, v109, 16, 16
	v_lshl_or_b32 v209, v209, 7, v113
	global_load_dwordx4 v[44:47], v209, s[64:65]
	s_lshl_b32 s78, s33, 8
	v_add_u32_e32 v123, s78, v112
	ds_read_b64 v[108:109], v123 offset:192
	s_waitcnt lgkmcnt(0)
	v_lshlrev_b32_e32 v208, 7, v108
	v_and_or_b32 v208, v208, s77, v113
	global_load_dwordx4 v[48:51], v208, s[64:65]
	v_bfe_u32 v209, v108, 16, 16
	v_lshl_or_b32 v209, v209, 7, v113
	global_load_dwordx4 v[52:55], v209, s[64:65]
	v_lshlrev_b32_e32 v208, 7, v109
	v_and_or_b32 v208, v208, s77, v113
	global_load_dwordx4 v[56:59], v208, s[64:65]
	v_bfe_u32 v209, v109, 16, 16
	v_lshl_or_b32 v209, v209, 7, v113
	global_load_dwordx4 v[60:63], v209, s[64:65]
	s_ashr_i32 s55, s8, 31
	s_mov_b32 s54, s8
	s_lshl_b64 s[54:55], s[54:55], 12
	s_add_u32 s54, s90, s54
	s_addc_u32 s55, s91, s55
	s_lshl_b32 s78, s58, 9
	s_add_u32 s54, s54, s78
	s_addc_u32 s55, s55, 0
	v_lshl_add_u64 v[208:209], s[54:55], 0, v[184:185]
	global_load_dwordx2 v[172:173], v[208:209], off
; #define LAS __attribute__((address_space(3)))
; __device__ __forceinline__ void expert_phase(const Frame& F, int l, int xcc, LAS unsigned char* wl, const LAS unsigned char* zb) {
;     ...
;                 const u32x4 ia = *(const LAS u32x4*)(IDL + (i & 7) * 256 + rr * 32), ib = *(const LAS u32x4*)(IDL + (i & 7) * 256 + rr * 32 + 16);
; #pragma unroll
;                 for (int j = 0; j < 16; ++j) { const unsigned w = j < 8 ? ia[(j >> 1) & 3] : ib[(j >> 1) & 3]; const unsigned e = (j & 1) ? (w >> 16) : (w & 0xffffu);
;                     R.r[j] = ldo_u4(Vsl, e * 128u + 16u * pc); }
;             };
;             auto v_comp = [&](int i, const URows& R) {
;                 const int k = i & 7, t = tok(k), sl = slice_of(i);
;                 const unsigned col = 32u * pc + 4u * rr;
;                 u32x2 xw;
;                 typedef _Float16 hf2 __attribute__((ext_vector_type(2)));
;                 const LAS u32x4* wp = (const LAS u32x4*)(SA + k * 256 + 16 * rr);
;                 const u32x4 wall[4] = {wp[0], wp[1], wp[2], wp[3]};
;                 unsigned out[16];
; #pragma unroll
;                 for (int j = 0; j < 16; ++j) out[j] = 0u;
; #pragma unroll
;                 for (int j = 0; j < 16; ++j) {
;                     if (j == 8) xw = ldo_u2(X1 + (size_t)t * D + sl * 256, 2u * col);
;                     u32x4 rj = R.r[j];
;                     asm volatile("" : "+v"(rj.x), "+v"(rj.y), "+v"(rj.z), "+v"(rj.w) :: "memory");
;                     const unsigned wj = wall[j >> 2][j & 3]; const hf2 w2 = __builtin_bit_cast(hf2, wj);
; #pragma unroll
;                     for (int d = 0; d < 4; ++d) {
;                         const hf2 a = __builtin_amdgcn_cvt_scalef32_pk_f16_fp4(rj[d], 1.0f, 0), b = __builtin_amdgcn_cvt_scalef32_pk_f16_fp4(rj[d], 1.0f, 1),
;                                   cc = __builtin_amdgcn_cvt_scalef32_pk_f16_fp4(rj[d], 1.0f, 2), dd = __builtin_amdgcn_cvt_scalef32_pk_f16_fp4(rj[d], 1.0f, 3);
;                         out[4 * d] = __builtin_bit_cast(unsigned, __builtin_elementwise_fma(a, w2, __builtin_bit_cast(hf2, out[4 * d])));
;                         out[4 * d + 1] = __builtin_bit_cast(unsigned, __builtin_elementwise_fma(b, w2, __builtin_bit_cast(hf2, out[4 * d + 1])));
;                         out[4 * d + 2] = __builtin_bit_cast(unsigned, __builtin_elementwise_fma(cc, w2, __builtin_bit_cast(hf2, out[4 * d + 2])));
.Lv_loop:
	s_and_b32 s2, s67, 7
	s_lshr_b32 s3, s67, 3
	s_add_i32 s3, s3, s96
	s_and_b32 s3, s3, 7
	s_mul_i32 s8, s2, s82
	s_add_i32 s8, s8, s26
	s_cmpk_lt_i32 s8, 0x4000
	s_cselect_b32 s8, s8, s26
	s_add_i32 s4, s67, 1
	s_min_i32 s4, s4, 63
	s_and_b32 s33, s4, 7
	s_lshr_b32 s58, s4, 3
	s_add_i32 s58, s58, s96
	s_and_b32 s58, s58, 7
	s_mul_i32 s9, s33, s82
	s_add_i32 s9, s9, s26
	s_cmpk_lt_i32 s9, 0x4000
	s_cselect_b32 s9, s9, s26
	s_lshl_b32 s78, s58, 21
	s_add_u32 s64, s57, s78
	s_addc_u32 s65, s70, 0
	s_lshl_b32 s5, s2, 10
	s_waitcnt vmcnt(13)
	ds_write_b128 v110, v[0:3] offset:0
	ds_write_b128 v110, v[4:7] offset:144
	ds_write_b128 v110, v[8:11] offset:288
	ds_write_b128 v110, v[12:15] offset:432
	s_add_i32 s78, s5, 0
	v_add_u32_e32 v120, s78, v114
	v_mov_b32_e32 v121, 0x1a000
	v_cndmask_b32_e64 v122, v121, v120, s[30:31]
	v_cndmask_b32_e64 v121, v121, v120, s[44:45]
	ds_read_b128 v[80:83], v122
	ds_read_b128 v[84:87], v121
	s_lshl_b32 s78, s33, 8
	v_add_u32_e32 v123, s78, v112
	ds_read_b64 v[108:109], v123 offset:0
	ds_read_b64_tr_b4 v[64:65], v111 offset:0
	ds_read_b64_tr_b4 v[66:67], v111 offset:2304
	ds_read_b64_tr_b4 v[68:69], v111 offset:32
	ds_read_b64_tr_b4 v[70:71], v111 offset:2336
	ds_read_b64_tr_b4 v[72:73], v111 offset:64
	ds_read_b64_tr_b4 v[74:75], v111 offset:2368
	ds_read_b64_tr_b4 v[76:77], v111 offset:96
	ds_read_b64_tr_b4 v[78:79], v111 offset:2400
	s_waitcnt lgkmcnt(8)
	v_lshlrev_b32_e32 v208, 7, v108
	v_and_or_b32 v208, v208, s77, v113
	global_load_dwordx4 v[0:3], v208, s[64:65]
	v_bfe_u32 v209, v108, 16, 16
	v_lshl_or_b32 v209, v209, 7, v113
	global_load_dwordx4 v[4:7], v209, s[64:65]
	v_lshlrev_b32_e32 v208, 7, v109
	v_and_or_b32 v208, v208, s77, v113
	global_load_dwordx4 v[8:11], v208, s[64:65]
	v_bfe_u32 v209, v109, 16, 16
	v_lshl_or_b32 v209, v209, 7, v113
	global_load_dwordx4 v[12:15], v209, s[64:65]
	s_waitcnt lgkmcnt(0)
	v_mfma_scale_f32_16x16x128_f8f6f4 v[88:91], v[64:67], v[80:87], 0, v215, v215 op_sel_hi:[0,0,0] cbsz:4
	v_mfma_scale_f32_16x16x128_f8f6f4 v[92:95], v[68:71], v[80:87], 0, v215, v215 op_sel_hi:[0,0,0] cbsz:4
	v_mfma_scale_f32_16x16x128_f8f6f4 v[96:99], v[72:75], v[80:87], 0, v215, v215 op_sel_hi:[0,0,0] cbsz:4
	v_mfma_scale_f32_16x16x128_f8f6f4 v[100:103], v[76:79], v[80:87], 0, v215, v215 op_sel_hi:[0,0,0] cbsz:4
	s_waitcnt vmcnt(13)
	ds_write_b128 v110, v[16:19] offset:0
	ds_write_b128 v110, v[20:23] offset:144
	ds_write_b128 v110, v[24:27] offset:288
	ds_write_b128 v110, v[28:31] offset:432
	s_add_i32 s78, s5, 32
	v_add_u32_e32 v120, s78, v114
	v_mov_b32_e32 v121, 0x1a000
	v_cndmask_b32_e64 v122, v121, v120, s[30:31]
	v_cndmask_b32_e64 v121, v121, v120, s[44:45]
	ds_read_b128 v[80:83], v122
	ds_read_b128 v[84:87], v121
	s_lshl_b32 s78, s33, 8
	v_add_u32_e32 v123, s78, v112
	ds_read_b64 v[108:109], v123 offset:64
	ds_read_b64_tr_b4 v[64:65], v111 offset:0
	ds_read_b64_tr_b4 v[66:67], v111 offset:2304
	ds_read_b64_tr_b4 v[68:69], v111 offset:32
	ds_read_b64_tr_b4 v[70:71], v111 offset:2336
	ds_read_b64_tr_b4 v[72:73], v111 offset:64
	ds_read_b64_tr_b4 v[74:75], v111 offset:2368
	ds_read_b64_tr_b4 v[76:77], v111 offset:96
	ds_read_b64_tr_b4 v[78:79], v111 offset:2400
	s_waitcnt lgkmcnt(8)
	v_lshlrev_b32_e32 v208, 7, v108
	v_and_or_b32 v208, v208, s77, v113
	global_load_dwordx4 v[16:19], v208, s[64:65]
	v_bfe_u32 v209, v108, 16, 16
	v_lshl_or_b32 v209, v209, 7, v113
	global_load_dwordx4 v[20:23], v209, s[64:65]
	v_lshlrev_b32_e32 v208, 7, v109
	v_and_or_b32 v208, v208, s77, v113
	global_load_dwordx4 v[24:27], v208, s[64:65]
	v_bfe_u32 v209, v109, 16, 16
	v_lshl_or_b32 v209, v209, 7, v113
	global_load_dwordx4 v[28:31], v209, s[64:65]
	s_waitcnt lgkmcnt(0)
	v_mfma_scale_f32_16x16x128_f8f6f4 v[88:91], v[64:67], v[80:87], v[88:91], v215, v215 op_sel_hi:[0,0,0] cbsz:4
	v_mfma_scale_f32_16x16x128_f8f6f4 v[92:95], v[68:71], v[80:87], v[92:95], v215, v215 op_sel_hi:[0,0,0] cbsz:4
	v_mfma_scale_f32_16x16x128_f8f6f4 v[96:99], v[72:75], v[80:87], v[96:99], v215, v215 op_sel_hi:[0,0,0] cbsz:4
	v_mfma_scale_f32_16x16x128_f8f6f4 v[100:103], v[76:79], v[80:87], v[100:103], v215, v215 op_sel_hi:[0,0,0] cbsz:4
	s_waitcnt vmcnt(13)
	ds_write_b128 v110, v[32:35] offset:0
	ds_write_b128 v110, v[36:39] offset:144
	ds_write_b128 v110, v[40:43] offset:288
	ds_write_b128 v110, v[44:47] offset:432
	s_add_i32 s78, s5, 64
	v_add_u32_e32 v120, s78, v114
	v_mov_b32_e32 v121, 0x1a000
	v_cndmask_b32_e64 v122, v121, v120, s[30:31]
	v_cndmask_b32_e64 v121, v121, v120, s[44:45]
	ds_read_b128 v[80:83], v122
	ds_read_b128 v[84:87], v121
	s_lshl_b32 s78, s33, 8
	v_add_u32_e32 v123, s78, v112
	ds_read_b64 v[108:109], v123 offset:128
	ds_read_b64_tr_b4 v[64:65], v111 offset:0
	ds_read_b64_tr_b4 v[66:67], v111 offset:2304
	ds_read_b64_tr_b4 v[68:69], v111 offset:32
	ds_read_b64_tr_b4 v[70:71], v111 offset:2336
	ds_read_b64_tr_b4 v[72:73], v111 offset:64
	ds_read_b64_tr_b4 v[74:75], v111 offset:2368
	ds_read_b64_tr_b4 v[76:77], v111 offset:96
	ds_read_b64_tr_b4 v[78:79], v111 offset:2400
	s_waitcnt lgkmcnt(8)
	v_lshlrev_b32_e32 v208, 7, v108
	v_and_or_b32 v208, v208, s77, v113
	global_load_dwordx4 v[32:35], v208, s[64:65]
	v_bfe_u32 v209, v108, 16, 16
	v_lshl_or_b32 v209, v209, 7, v113
	global_load_dwordx4 v[36:39], v209, s[64:65]
	v_lshlrev_b32_e32 v208, 7, v109
	v_and_or_b32 v208, v208, s77, v113
	global_load_dwordx4 v[40:43], v208, s[64:65]
	v_bfe_u32 v209, v109, 16, 16
	v_lshl_or_b32 v209, v209, 7, v113
	global_load_dwordx4 v[44:47], v209, s[64:65]
	s_waitcnt lgkmcnt(0)
; __device__ __forceinline__ unsigned pk2(float lo, float hi) { return f2bf(lo) | (f2bf(hi) << 16); }
; __device__ __forceinline__ void expert_phase(const Frame& F, int l, int xcc, LAS unsigned char* wl, const LAS unsigned char* zb) {
;     ...
;                 unsigned o2[2];
;                 {
;                     const bool b5 = (lane & 32) != 0, b4 = (lane & 16) != 0, b3 = (lane & 8) != 0;
;                     unsigned q8[8], q4[4];
;                     auto hadd = [](unsigned x, unsigned y) { return __builtin_bit_cast(unsigned, __builtin_bit_cast(hf2, x) + __builtin_bit_cast(hf2, y)); };
; #pragma unroll
;                     for (int n = 0; n < 8; ++n) { const unsigned send = b5 ? out[n] : out[n + 8], keep = b5 ? out[n + 8] : out[n]; q8[n] = hadd(keep, (unsigned)__shfl_xor((int)send, 32)); }
; #pragma unroll
;                     for (int n = 0; n < 4; ++n) { const unsigned send = b4 ? q8[n] : q8[n + 4], keep = b4 ? q8[n + 4] : q8[n]; q4[n] = hadd(keep, (unsigned)__shfl_xor((int)send, 16)); }
; #pragma unroll
;                     for (int n = 0; n < 2; ++n) { const unsigned send = b3 ? q4[n] : q4[n + 2], keep = b3 ? q4[n + 2] : q4[n]; o2[n] = hadd(keep, (unsigned)__shfl_xor((int)send, 8)); }
;                 }
;                 const float isc = RS[8 + k];
;                 const hf2 oa = __builtin_bit_cast(hf2, o2[0]), ob = __builtin_bit_cast(hf2, o2[1]);
;                 const float y0 = bf_lo(xw.x) + (float)oa[0] * isc, y1 = bf_hi(xw.x) + (float)oa[1] * isc, y2 = bf_lo(xw.y) + (float)ob[0] * isc, y3 = bf_hi(xw.y) + (float)ob[1] * isc;
;                 if (l + 1 < DEPTH) {
;                     u32x2 w; w.x = pk2(y0, y1); w.y = pk2(y2, y3);
;                     sto_u2(XR + (size_t)t * D + sl * 256, 2u * col, w);
;                     const float s = (y0 * y0 + y1 * y1) + (y2 * y2 + y3 * y3);
;                     (void)__hip_atomic_fetch_add(SQ + k * 64 + lane, s, __ATOMIC_RELAXED, __HIP_MEMORY_SCOPE_WAVEFRONT);
;                 } else sto_f4(F.out + (size_t)t * D + sl * 256, 4u * col, (f32x4){y0, y1, y2, y3});
	v_mfma_scale_f32_16x16x128_f8f6f4 v[88:91], v[64:67], v[80:87], v[88:91], v215, v215 op_sel_hi:[0,0,0] cbsz:4
	v_mfma_scale_f32_16x16x128_f8f6f4 v[92:95], v[68:71], v[80:87], v[92:95], v215, v215 op_sel_hi:[0,0,0] cbsz:4
	v_mfma_scale_f32_16x16x128_f8f6f4 v[96:99], v[72:75], v[80:87], v[96:99], v215, v215 op_sel_hi:[0,0,0] cbsz:4
	v_mfma_scale_f32_16x16x128_f8f6f4 v[100:103], v[76:79], v[80:87], v[100:103], v215, v215 op_sel_hi:[0,0,0] cbsz:4
	s_waitcnt vmcnt(13)
	ds_write_b128 v110, v[48:51] offset:0
	ds_write_b128 v110, v[52:55] offset:144
	ds_write_b128 v110, v[56:59] offset:288
	ds_write_b128 v110, v[60:63] offset:432
	s_add_i32 s78, s5, 96
	v_add_u32_e32 v120, s78, v114
	v_mov_b32_e32 v121, 0x1a000
	v_cndmask_b32_e64 v122, v121, v120, s[30:31]
	v_cndmask_b32_e64 v121, v121, v120, s[44:45]
	ds_read_b128 v[80:83], v122
	ds_read_b128 v[84:87], v121
	s_lshl_b32 s78, s33, 8
	v_add_u32_e32 v123, s78, v112
	ds_read_b64 v[108:109], v123 offset:192
	ds_read_b64_tr_b4 v[64:65], v111 offset:0
	ds_read_b64_tr_b4 v[66:67], v111 offset:2304
	ds_read_b64_tr_b4 v[68:69], v111 offset:32
	ds_read_b64_tr_b4 v[70:71], v111 offset:2336
	ds_read_b64_tr_b4 v[72:73], v111 offset:64
	ds_read_b64_tr_b4 v[74:75], v111 offset:2368
	ds_read_b64_tr_b4 v[76:77], v111 offset:96
	ds_read_b64_tr_b4 v[78:79], v111 offset:2400
	s_waitcnt lgkmcnt(8)
	v_lshlrev_b32_e32 v208, 7, v108
	v_and_or_b32 v208, v208, s77, v113
	global_load_dwordx4 v[48:51], v208, s[64:65]
	v_bfe_u32 v209, v108, 16, 16
	v_lshl_or_b32 v209, v209, 7, v113
	global_load_dwordx4 v[52:55], v209, s[64:65]
	v_lshlrev_b32_e32 v208, 7, v109
	v_and_or_b32 v208, v208, s77, v113
	global_load_dwordx4 v[56:59], v208, s[64:65]
	v_bfe_u32 v209, v109, 16, 16
	v_lshl_or_b32 v209, v209, 7, v113
	global_load_dwordx4 v[60:63], v209, s[64:65]
	s_waitcnt lgkmcnt(0)
	v_mfma_scale_f32_16x16x128_f8f6f4 v[88:91], v[64:67], v[80:87], v[88:91], v215, v215 op_sel_hi:[0,0,0] cbsz:4
	v_mfma_scale_f32_16x16x128_f8f6f4 v[92:95], v[68:71], v[80:87], v[92:95], v215, v215 op_sel_hi:[0,0,0] cbsz:4
	v_mfma_scale_f32_16x16x128_f8f6f4 v[96:99], v[72:75], v[80:87], v[96:99], v215, v215 op_sel_hi:[0,0,0] cbsz:4
	v_mfma_scale_f32_16x16x128_f8f6f4 v[100:103], v[76:79], v[80:87], v[100:103], v215, v215 op_sel_hi:[0,0,0] cbsz:4
	s_ashr_i32 s55, s8, 31
	s_mov_b32 s54, s8
	s_lshl_b64 s[54:55], s[54:55], 12
	s_lshl_b32 s78, s3, 9
	s_add_u32 s4, s48, s54
	s_addc_u32 s5, s49, s55
	s_add_u32 s4, s4, s78
	s_addc_u32 s5, s5, 0
	s_lshl_b32 s78, s2, 2
	s_add_i32 s78, s78, s83
	v_mov_b32_e32 v120, s78
	s_lshl_b32 s78, s2, 8
	v_add_u32_e32 v121, s78, v117
	ds_read_b32 v122, v120 offset:10272
	ds_read_b32 v123, v121
	s_nop 4
	v_add_f32_dpp v88, v88, v88 row_shl:4 row_mask:0xf bank_mask:0xf
	v_add_f32_dpp v89, v89, v89 row_shl:4 row_mask:0xf bank_mask:0xf
	v_add_f32_dpp v90, v90, v90 row_shl:4 row_mask:0xf bank_mask:0xf
	v_add_f32_dpp v91, v91, v91 row_shl:4 row_mask:0xf bank_mask:0xf
	v_add_f32_dpp v92, v92, v92 row_shl:4 row_mask:0xf bank_mask:0xf
	v_add_f32_dpp v93, v93, v93 row_shl:4 row_mask:0xf bank_mask:0xf
	v_add_f32_dpp v94, v94, v94 row_shl:4 row_mask:0xf bank_mask:0xf
	v_add_f32_dpp v95, v95, v95 row_shl:4 row_mask:0xf bank_mask:0xf
	v_add_f32_dpp v96, v96, v96 row_shl:4 row_mask:0xf bank_mask:0xf
	v_add_f32_dpp v97, v97, v97 row_shl:4 row_mask:0xf bank_mask:0xf
	v_add_f32_dpp v98, v98, v98 row_shl:4 row_mask:0xf bank_mask:0xf
	v_add_f32_dpp v99, v99, v99 row_shl:4 row_mask:0xf bank_mask:0xf
	v_add_f32_dpp v100, v100, v100 row_shl:4 row_mask:0xf bank_mask:0xf
	v_add_f32_dpp v101, v101, v101 row_shl:4 row_mask:0xf bank_mask:0xf
	v_add_f32_dpp v102, v102, v102 row_shl:4 row_mask:0xf bank_mask:0xf
	v_add_f32_dpp v103, v103, v103 row_shl:4 row_mask:0xf bank_mask:0xf
	v_add_f32_dpp v88, v88, v88 row_shl:8 row_mask:0xf bank_mask:0xf
	v_add_f32_dpp v89, v89, v89 row_shl:8 row_mask:0xf bank_mask:0xf
	v_add_f32_dpp v90, v90, v90 row_shl:8 row_mask:0xf bank_mask:0xf
	v_add_f32_dpp v91, v91, v91 row_shl:8 row_mask:0xf bank_mask:0xf
	v_add_f32_dpp v92, v92, v92 row_shl:8 row_mask:0xf bank_mask:0xf
	v_add_f32_dpp v93, v93, v93 row_shl:8 row_mask:0xf bank_mask:0xf
	v_add_f32_dpp v94, v94, v94 row_shl:8 row_mask:0xf bank_mask:0xf
	v_add_f32_dpp v95, v95, v95 row_shl:8 row_mask:0xf bank_mask:0xf
	v_add_f32_dpp v96, v96, v96 row_shl:8 row_mask:0xf bank_mask:0xf
	v_add_f32_dpp v97, v97, v97 row_shl:8 row_mask:0xf bank_mask:0xf
	v_add_f32_dpp v98, v98, v98 row_shl:8 row_mask:0xf bank_mask:0xf
	v_add_f32_dpp v99, v99, v99 row_shl:8 row_mask:0xf bank_mask:0xf
	v_add_f32_dpp v100, v100, v100 row_shl:8 row_mask:0xf bank_mask:0xf
	v_add_f32_dpp v101, v101, v101 row_shl:8 row_mask:0xf bank_mask:0xf
	v_add_f32_dpp v102, v102, v102 row_shl:8 row_mask:0xf bank_mask:0xf
	v_add_f32_dpp v103, v103, v103 row_shl:8 row_mask:0xf bank_mask:0xf
	s_mov_b64 exec, s[100:101]
	ds_write_b128 v115, v[88:91] offset:0
	ds_write_b128 v115, v[92:95] offset:256
	ds_write_b128 v115, v[96:99] offset:512
	ds_write_b128 v115, v[100:103] offset:768
	s_mov_b64 exec, -1
	ds_read_b128 v[104:107], v116
	s_waitcnt vmcnt(16) lgkmcnt(0)
	v_lshlrev_b32_e32 v124, 16, v172
	v_and_b32_e32 v125, 0xffff0000, v172
	v_lshlrev_b32_e32 v126, 16, v173
	v_and_b32_e32 v127, 0xffff0000, v173
	v_fma_f32 v124, v104, v122, v124
	v_fma_f32 v125, v105, v122, v125
	v_fma_f32 v126, v106, v122, v126
	v_fma_f32 v127, v107, v122, v127
	s_ashr_i32 s55, s9, 31
	s_mov_b32 s54, s9
	s_lshl_b64 s[54:55], s[54:55], 12
	s_add_u32 s54, s90, s54
	s_addc_u32 s55, s91, s55
	s_lshl_b32 s78, s58, 9
	s_add_u32 s54, s54, s78
	s_addc_u32 s55, s55, 0
	v_lshl_add_u64 v[208:209], s[54:55], 0, v[184:185]
	global_load_dwordx2 v[172:173], v[208:209], off
	s_and_b64 vcc, exec, s[20:21]
	s_cbranch_vccz .Lv_last
	v_bfe_u32 v128, v124, 16, 1
	v_bfe_u32 v129, v125, 16, 1
	v_bfe_u32 v130, v126, 16, 1
	v_bfe_u32 v131, v127, 16, 1
	v_add3_u32 v128, v124, v128, s68
	v_add3_u32 v129, v125, v129, s68
	v_add3_u32 v130, v126, v130, s68
	v_add3_u32 v131, v127, v131, s68
	v_perm_b32 v132, v129, v128, s66
	v_perm_b32 v133, v131, v130, s66
	v_lshl_add_u64 v[208:209], s[4:5], 0, v[184:185]
	global_store_dwordx2 v[208:209], v[132:133], off
	v_mul_f32_e32 v134, v124, v124
	v_fmac_f32_e32 v134, v125, v125
	v_fmac_f32_e32 v134, v126, v126
	v_fmac_f32_e32 v134, v127, v127
	v_add_f32_e32 v123, v123, v134
	ds_write_b32 v121, v123
	s_branch .Lv_next
; #define GAS __attribute__((address_space(1)))
; __device__ __forceinline__ float frsq(float x) { return __builtin_amdgcn_rsqf(x); }
; #define XFENCE() asm volatile("" ::: "memory")
; __device__ __forceinline__ void expert_phase(const Frame& F, int l, int xcc, LAS unsigned char* wl, const LAS unsigned char* zb) {
;     ...
;                 } else sto_f4(F.out + (size_t)t * D + sl * 256, 4u * col, (f32x4){y0, y1, y2, y3});
;             };
;             URows RA, RB;
;             v_rows(0, RA);
;             XFENCE();
; #pragma unroll 1
;             for (int i = 0; i < 64; i += 2) {
;                 const int i2 = i + 2 < 64 ? i + 2 : 63;
;                 v_rows(i + 1, RB);
;                 XFENCE();
;                 v_comp(i, RA);
;                 XFENCE();
;                 v_rows(i2, RA);
;                 XFENCE();
;                 v_comp(i + 1, RB);
;                 XFENCE();
;             }
;         }
;         if (l + 1 < DEPTH) {
;             float* RSTD = (float*)(F.ws + WS_RSTD);
; #pragma unroll
;             for (int k = 0; k < 8; ++k) { const float r1 = frsq(wave_sum(SQ[k * 64 + lane]) * (1.f / D) + EPS); if (lane == 0) *(GAS float*)(RSTD + tok(k)) = r1; }
.Lv_last:
	s_ashr_i32 s55, s8, 31
	s_mov_b32 s54, s8
	s_lshl_b64 s[54:55], s[54:55], 13
	s_lshl_b32 s78, s3, 10
	s_add_u32 s4, s60, s54
	s_addc_u32 s5, s61, s55
	s_add_u32 s4, s4, s78
	s_addc_u32 s5, s5, 0
	v_lshlrev_b32_e32 v208, 4, v211
	v_mov_b32_e32 v209, 0
	v_lshl_add_u64 v[208:209], s[4:5], 0, v[208:209]
	v_mov_b32_e32 v128, v124
	v_mov_b32_e32 v129, v125
	v_mov_b32_e32 v130, v126
	v_mov_b32_e32 v131, v127
	global_store_dwordx4 v[208:209], v[128:131], off
.Lv_next:
	s_add_i32 s67, s67, 1
	s_cmp_lt_i32 s67, 64
	s_cbranch_scc1 .Lv_loop
	s_waitcnt vmcnt(0) lgkmcnt(0)
.LBB0_1249:
	s_waitcnt vmcnt(0)
	s_and_b64 vcc, exec, s[20:21]
	s_cbranch_vccz .LBB0_1124
	ds_read_b32 v0, v201 offset:8192
	s_waitcnt lgkmcnt(0)
	ds_bpermute_b32 v1, v176, v0
	s_waitcnt lgkmcnt(0)
	v_add_f32_e32 v0, v0, v1
	ds_bpermute_b32 v1, v177, v0
	s_waitcnt lgkmcnt(0)
	v_add_f32_e32 v0, v0, v1
	ds_bpermute_b32 v1, v178, v0
	s_waitcnt lgkmcnt(0)
	v_add_f32_e32 v0, v0, v1
	ds_bpermute_b32 v1, v179, v0
	s_waitcnt lgkmcnt(0)
	v_add_f32_e32 v0, v0, v1
	ds_bpermute_b32 v1, v180, v0
	s_waitcnt lgkmcnt(0)
	v_add_f32_e32 v0, v0, v1
	ds_bpermute_b32 v1, v181, v0
	s_and_saveexec_b64 s[2:3], s[34:35]
	s_cbranch_execz .LBB0_1252
	s_waitcnt lgkmcnt(0)
	v_add_f32_e32 v0, v0, v1
	v_fmamk_f32 v0, v0, 0x3a000000, v214
	v_rsq_f32_e32 v0, v0
	s_lshl_b64 s[4:5], s[26:27], 2
	v_readlane_b32 s8, v250, 22
	v_readlane_b32 s9, v250, 23
	s_add_u32 s4, s8, s4
	s_addc_u32 s5, s9, s5
	global_store_dword v185, v0, s[4:5]

; __global__ void __launch_bounds__(NWAVES * 64, 2) hybrid_fwd(Args args) {
;     extern __shared__ __attribute__((aligned(16))) unsigned char lds_raw[];
	.amdhsa_kernel _Z10hybrid_fwd4Args
		.amdhsa_group_segment_fixed_size 9216
		.amdhsa_private_segment_fixed_size 0
		.amdhsa_kernarg_size 400
		.amdhsa_user_sgpr_count 2
		.amdhsa_user_sgpr_dispatch_ptr 0
		.amdhsa_user_sgpr_queue_ptr 0
		.amdhsa_user_sgpr_kernarg_segment_ptr 1
		.amdhsa_user_sgpr_dispatch_id 0
		.amdhsa_user_sgpr_kernarg_preload_length 0
		.amdhsa_user_sgpr_kernarg_preload_offset 0
		.amdhsa_user_sgpr_private_segment_size 0
		.amdhsa_uses_dynamic_stack 0
		.amdhsa_enable_private_segment 0
		.amdhsa_system_sgpr_workgroup_id_x 1
		.amdhsa_system_sgpr_workgroup_id_y 0
		.amdhsa_system_sgpr_workgroup_id_z 0
		.amdhsa_system_sgpr_workgroup_info 0
		.amdhsa_system_vgpr_workitem_id 0
		.amdhsa_next_free_vgpr 254
		.amdhsa_next_free_sgpr 102
		.amdhsa_accum_offset 256
		.amdhsa_reserve_vcc 1
		.amdhsa_float_round_mode_32 0
		.amdhsa_float_round_mode_16_64 0
		.amdhsa_float_denorm_mode_32 3
		.amdhsa_float_denorm_mode_16_64 3
		.amdhsa_dx10_clamp 1
		.amdhsa_ieee_mode 1
		.amdhsa_fp16_overflow 0
		.amdhsa_tg_split 0
		.amdhsa_exception_fp_ieee_invalid_op 0
		.amdhsa_exception_fp_denorm_src 0
		.amdhsa_exception_fp_ieee_div_zero 0
		.amdhsa_exception_fp_ieee_overflow 0
		.amdhsa_exception_fp_ieee_underflow 0
		.amdhsa_exception_fp_ieee_inexact 0
		.amdhsa_exception_int_div_zero 0
	.end_amdhsa_kernel

; __global__ void __launch_bounds__(NWAVES * 64, 2) hybrid_fwd(Args args) {
;     extern __shared__ __attribute__((aligned(16))) unsigned char lds_raw[];
amdhsa.kernels:
  - .agpr_count:     0
    .args:
      - .offset:         0
        .size:           144
        .value_kind:     by_value
      - .offset:         144
        .size:           4
        .value_kind:     hidden_block_count_x
      - .offset:         148
        .size:           4
        .value_kind:     hidden_block_count_y
      - .offset:         152
        .size:           4
        .value_kind:     hidden_block_count_z
      - .offset:         156
        .size:           2
        .value_kind:     hidden_group_size_x
      - .offset:         158
        .size:           2
        .value_kind:     hidden_group_size_y
      - .offset:         160
        .size:           2
        .value_kind:     hidden_group_size_z
      - .offset:         162
        .size:           2
        .value_kind:     hidden_remainder_x
      - .offset:         164
        .size:           2
        .value_kind:     hidden_remainder_y
      - .offset:         166
        .size:           2
        .value_kind:     hidden_remainder_z
      - .offset:         184
        .size:           8
        .value_kind:     hidden_global_offset_x
      - .offset:         192
        .size:           8
        .value_kind:     hidden_global_offset_y
      - .offset:         200
        .size:           8
        .value_kind:     hidden_global_offset_z
      - .offset:         208
        .size:           2
        .value_kind:     hidden_grid_dims
      - .offset:         264
        .size:           4
        .value_kind:     hidden_dynamic_lds_size
    .group_segment_fixed_size: 9216
    .kernarg_segment_align: 8
    .kernarg_segment_size: 400
    .language:       OpenCL C
    .language_version:
      - 2
      - 0
    .max_flat_workgroup_size: 512
    .name:           _Z10hybrid_fwd4Args
    .private_segment_fixed_size: 0
    .sgpr_count:     108
    .sgpr_spill_count: 243
    .symbol:         _Z10hybrid_fwd4Args.kd
    .uniform_work_group_size: 1
    .uses_dynamic_stack: false
    .vgpr_count:     254
    .vgpr_spill_count: 0
    .wavefront_size: 64
